# conv mixer GLU staging loop unrolled by hand: all ten row loads issued up front instead of ten serialised load-wait round trips
# baseline (speedup 1.0000x reference)
.LBB0_831:
	v_readlane_b32 s16, v242, 31
	s_and_b32 s10, s86, 3
	v_readlane_b32 s17, v242, 32
	s_and_saveexec_b64 s[4:5], s[16:17]
	s_xor_b64 s[4:5], exec, s[4:5]
	s_lshl_b32 s46, s10, 7
	s_or_saveexec_b64 s[4:5], s[4:5]
	s_lshl_b32 s11, s86, 5
	s_and_b32 s87, s11, 0xffffff80
	v_mov_b32_e32 v6, s46
	v_mov_b64_e32 v[28:29], s[46:47]
	s_xor_b64 exec, exec, s[4:5]
	s_cbranch_execz .LBB0_830
	s_and_b32 s11, s11, 0x780
	s_mov_b32 s16, s75
	s_sub_i32 s75, 29, s11
	s_lshl_b32 s46, s10, 7
	s_lshl_b32 s10, s10, 8
	s_mov_b32 s11, s47
	s_sub_i32 s89, s87, 30
	v_lshl_add_u64 v[12:13], v[20:21], 0, s[10:11]
	s_mov_b64 s[10:11], 0
	v_ashrrev_i32_e32 v15, 4, v54
	v_add_u32_e32 v28, s89, v15
	v_mad_i64_i32 v[234:235], vcc, v28, s74, v[12:13]
	v_lshl_add_u32 v187, v15, 9, v41
	s_movk_i32 s99, 0x1e0
	v_add_co_u32_e32 v236, vcc, 0x1000, v234
	s_nop 1
	v_addc_co_u32_e32 v237, vcc, 0, v235, vcc
	v_mov_b32_e32 v188, 0
	v_mov_b32_e32 v226, 0
	v_mov_b32_e32 v189, 0
	v_mov_b32_e32 v227, 0
	v_mov_b32_e32 v190, 0
	v_mov_b32_e32 v228, 0
	v_mov_b32_e32 v191, 0
	v_mov_b32_e32 v229, 0
	v_cmp_lt_i32_e32 vcc, s75, v15
	s_and_saveexec_b64 s[80:81], vcc
	global_load_dwordx4 v[188:191], v[234:235], off offset:3072
	global_load_dwordx4 v[226:229], v[236:237], off
	s_mov_b64 exec, s[80:81]
	v_add_co_u32_e32 v234, vcc, 0x30000, v234
	s_nop 1
	v_addc_co_u32_e32 v235, vcc, 0, v235, vcc
	v_add_co_u32_e32 v236, vcc, 0x30000, v236
	s_nop 1
	v_addc_co_u32_e32 v237, vcc, 0, v237, vcc
	v_mov_b32_e32 v192, 0
	v_mov_b32_e32 v230, 0
	v_mov_b32_e32 v193, 0
	v_mov_b32_e32 v231, 0
	v_mov_b32_e32 v194, 0
	v_mov_b32_e32 v232, 0
	v_mov_b32_e32 v195, 0
	v_mov_b32_e32 v233, 0
	s_sub_i32 s98, s75, 32
	v_cmp_lt_i32_e32 vcc, s98, v15
	s_and_saveexec_b64 s[80:81], vcc
	global_load_dwordx4 v[192:195], v[234:235], off offset:3072
	global_load_dwordx4 v[230:233], v[236:237], off
	s_mov_b64 exec, s[80:81]
	v_add_co_u32_e32 v234, vcc, 0x30000, v234
	s_nop 1
	v_addc_co_u32_e32 v235, vcc, 0, v235, vcc
	v_add_co_u32_e32 v236, vcc, 0x30000, v236
	s_nop 1
	v_addc_co_u32_e32 v237, vcc, 0, v237, vcc
	v_mov_b32_e32 v204, 0
	v_mov_b32_e32 v4, 0
	v_mov_b32_e32 v205, 0
	v_mov_b32_e32 v5, 0
	v_mov_b32_e32 v206, 0
	v_mov_b32_e32 v6, 0
	v_mov_b32_e32 v207, 0
	v_mov_b32_e32 v7, 0
	s_sub_i32 s98, s75, 64
	v_cmp_lt_i32_e32 vcc, s98, v15
	s_and_saveexec_b64 s[80:81], vcc
	global_load_dwordx4 v[204:207], v[234:235], off offset:3072
	global_load_dwordx4 v[4:7], v[236:237], off
	s_mov_b64 exec, s[80:81]
	v_add_co_u32_e32 v234, vcc, 0x30000, v234
	s_nop 1
	v_addc_co_u32_e32 v235, vcc, 0, v235, vcc
	v_add_co_u32_e32 v236, vcc, 0x30000, v236
	s_nop 1
	v_addc_co_u32_e32 v237, vcc, 0, v237, vcc
	v_mov_b32_e32 v208, 0
	v_mov_b32_e32 v8, 0
	v_mov_b32_e32 v209, 0
	v_mov_b32_e32 v9, 0
	v_mov_b32_e32 v210, 0
	v_mov_b32_e32 v10, 0
	v_mov_b32_e32 v211, 0
	v_mov_b32_e32 v11, 0
	s_sub_i32 s98, s75, 96
	v_cmp_lt_i32_e32 vcc, s98, v15
	s_and_saveexec_b64 s[80:81], vcc
	global_load_dwordx4 v[208:211], v[234:235], off offset:3072
	global_load_dwordx4 v[8:11], v[236:237], off
	s_mov_b64 exec, s[80:81]
	v_add_co_u32_e32 v234, vcc, 0x30000, v234
	s_nop 1
	v_addc_co_u32_e32 v235, vcc, 0, v235, vcc
	v_add_co_u32_e32 v236, vcc, 0x30000, v236
	s_nop 1
	v_addc_co_u32_e32 v237, vcc, 0, v237, vcc
	v_mov_b32_e32 v212, 0
	v_mov_b32_e32 v16, 0
	v_mov_b32_e32 v213, 0
	v_mov_b32_e32 v17, 0
	v_mov_b32_e32 v214, 0
	v_mov_b32_e32 v18, 0
	v_mov_b32_e32 v215, 0
	v_mov_b32_e32 v19, 0
	s_sub_i32 s98, s75, 128
	v_cmp_lt_i32_e32 vcc, s98, v15
	v_cmp_gt_i32_e64 s[80:81], s99, v54
	s_nop 1
	s_and_b64 vcc, vcc, s[80:81]
	s_and_saveexec_b64 s[80:81], vcc
	global_load_dwordx4 v[212:215], v[234:235], off offset:3072
	global_load_dwordx4 v[16:19], v[236:237], off
	s_mov_b64 exec, s[80:81]
	s_waitcnt vmcnt(8)
	v_lshlrev_b32_e32 v28, 16, v226
	v_and_b32_e32 v29, 0xffff0000, v226
	v_mul_f32_e32 v28, 0xbfb8aa3b, v28
	v_mul_f32_e32 v29, 0xbfb8aa3b, v29
	v_exp_f32_e32 v28, v28
	v_exp_f32_e32 v29, v29
	v_lshlrev_b32_e32 v30, 16, v188
	v_add_f32_e32 v28, 1.0, v28
	v_add_f32_e32 v29, 1.0, v29
	v_rcp_f32_e32 v28, v28
	v_rcp_f32_e32 v29, v29
	v_and_b32_e32 v31, 0xffff0000, v188
	v_mul_f32_e32 v12, v28, v30
	v_mul_f32_e32 v13, v29, v31
	v_lshlrev_b32_e32 v28, 16, v227
	v_and_b32_e32 v29, 0xffff0000, v227
	v_mul_f32_e32 v28, 0xbfb8aa3b, v28
	v_mul_f32_e32 v29, 0xbfb8aa3b, v29
	v_exp_f32_e32 v28, v28
	v_exp_f32_e32 v29, v29
	v_lshlrev_b32_e32 v30, 16, v189
	v_add_f32_e32 v28, 1.0, v28
	v_add_f32_e32 v29, 1.0, v29
	v_rcp_f32_e32 v28, v28
	v_rcp_f32_e32 v29, v29
	v_and_b32_e32 v31, 0xffff0000, v189
	v_mul_f32_e32 v14, v28, v30
	v_mul_f32_e32 v15, v29, v31
	v_lshlrev_b32_e32 v28, 16, v228
	v_and_b32_e32 v29, 0xffff0000, v228
	v_mul_f32_e32 v28, 0xbfb8aa3b, v28
	v_mul_f32_e32 v29, 0xbfb8aa3b, v29
	v_exp_f32_e32 v28, v28
	v_exp_f32_e32 v29, v29
	v_lshlrev_b32_e32 v30, 16, v190
	v_add_f32_e32 v28, 1.0, v28
	v_add_f32_e32 v29, 1.0, v29
	v_rcp_f32_e32 v28, v28
	v_rcp_f32_e32 v29, v29
	v_and_b32_e32 v31, 0xffff0000, v190
	v_mul_f32_e32 v238, v28, v30
	v_mul_f32_e32 v239, v29, v31
	v_lshlrev_b32_e32 v28, 16, v229
	v_and_b32_e32 v29, 0xffff0000, v229
	v_mul_f32_e32 v28, 0xbfb8aa3b, v28
	v_mul_f32_e32 v29, 0xbfb8aa3b, v29
	v_exp_f32_e32 v28, v28
	v_exp_f32_e32 v29, v29
	v_lshlrev_b32_e32 v30, 16, v191
	v_add_f32_e32 v28, 1.0, v28
	v_add_f32_e32 v29, 1.0, v29
	v_rcp_f32_e32 v28, v28
	v_rcp_f32_e32 v29, v29
	v_and_b32_e32 v31, 0xffff0000, v191
	v_mul_f32_e32 v240, v28, v30
	v_mul_f32_e32 v241, v29, v31
	ds_write_b128 v187, v[12:15]
	ds_write_b128 v187, v[238:241] offset:16
	v_add_u32_e32 v187, 0x4000, v187
	s_waitcnt vmcnt(6)
	v_lshlrev_b32_e32 v28, 16, v230
	v_and_b32_e32 v29, 0xffff0000, v230
	v_mul_f32_e32 v28, 0xbfb8aa3b, v28
	v_mul_f32_e32 v29, 0xbfb8aa3b, v29
	v_exp_f32_e32 v28, v28
	v_exp_f32_e32 v29, v29
	v_lshlrev_b32_e32 v30, 16, v192
	v_add_f32_e32 v28, 1.0, v28
	v_add_f32_e32 v29, 1.0, v29
	v_rcp_f32_e32 v28, v28
	v_rcp_f32_e32 v29, v29
	v_and_b32_e32 v31, 0xffff0000, v192
	v_mul_f32_e32 v12, v28, v30
	v_mul_f32_e32 v13, v29, v31
	v_lshlrev_b32_e32 v28, 16, v231
	v_and_b32_e32 v29, 0xffff0000, v231
	v_mul_f32_e32 v28, 0xbfb8aa3b, v28
	v_mul_f32_e32 v29, 0xbfb8aa3b, v29
	v_exp_f32_e32 v28, v28
	v_exp_f32_e32 v29, v29
	v_lshlrev_b32_e32 v30, 16, v193
	v_add_f32_e32 v28, 1.0, v28
	v_add_f32_e32 v29, 1.0, v29
	v_rcp_f32_e32 v28, v28
	v_rcp_f32_e32 v29, v29
	v_and_b32_e32 v31, 0xffff0000, v193
	v_mul_f32_e32 v14, v28, v30
	v_mul_f32_e32 v15, v29, v31
	v_lshlrev_b32_e32 v28, 16, v232
	v_and_b32_e32 v29, 0xffff0000, v232
	v_mul_f32_e32 v28, 0xbfb8aa3b, v28
	v_mul_f32_e32 v29, 0xbfb8aa3b, v29
	v_exp_f32_e32 v28, v28
	v_exp_f32_e32 v29, v29
	v_lshlrev_b32_e32 v30, 16, v194
	v_add_f32_e32 v28, 1.0, v28
	v_add_f32_e32 v29, 1.0, v29
	v_rcp_f32_e32 v28, v28
	v_rcp_f32_e32 v29, v29
	v_and_b32_e32 v31, 0xffff0000, v194
	v_mul_f32_e32 v238, v28, v30
	v_mul_f32_e32 v239, v29, v31
	v_lshlrev_b32_e32 v28, 16, v233
	v_and_b32_e32 v29, 0xffff0000, v233
	v_mul_f32_e32 v28, 0xbfb8aa3b, v28
	v_mul_f32_e32 v29, 0xbfb8aa3b, v29
	v_exp_f32_e32 v28, v28
	v_exp_f32_e32 v29, v29
	v_lshlrev_b32_e32 v30, 16, v195
	v_add_f32_e32 v28, 1.0, v28
	v_add_f32_e32 v29, 1.0, v29
	v_rcp_f32_e32 v28, v28
	v_rcp_f32_e32 v29, v29
	v_and_b32_e32 v31, 0xffff0000, v195
	v_mul_f32_e32 v240, v28, v30
	v_mul_f32_e32 v241, v29, v31
	ds_write_b128 v187, v[12:15]
	ds_write_b128 v187, v[238:241] offset:16
	v_add_u32_e32 v187, 0x4000, v187
	s_waitcnt vmcnt(4)
	v_lshlrev_b32_e32 v28, 16, v4
	v_and_b32_e32 v29, 0xffff0000, v4
	v_mul_f32_e32 v28, 0xbfb8aa3b, v28
	v_mul_f32_e32 v29, 0xbfb8aa3b, v29
	v_exp_f32_e32 v28, v28
	v_exp_f32_e32 v29, v29
	v_lshlrev_b32_e32 v30, 16, v204
	v_add_f32_e32 v28, 1.0, v28
	v_add_f32_e32 v29, 1.0, v29
	v_rcp_f32_e32 v28, v28
	v_rcp_f32_e32 v29, v29
	v_and_b32_e32 v31, 0xffff0000, v204
	v_mul_f32_e32 v12, v28, v30
	v_mul_f32_e32 v13, v29, v31
	v_lshlrev_b32_e32 v28, 16, v5
	v_and_b32_e32 v29, 0xffff0000, v5
	v_mul_f32_e32 v28, 0xbfb8aa3b, v28
	v_mul_f32_e32 v29, 0xbfb8aa3b, v29
	v_exp_f32_e32 v28, v28
	v_exp_f32_e32 v29, v29
	v_lshlrev_b32_e32 v30, 16, v205
	v_add_f32_e32 v28, 1.0, v28
	v_add_f32_e32 v29, 1.0, v29
	v_rcp_f32_e32 v28, v28
	v_rcp_f32_e32 v29, v29
	v_and_b32_e32 v31, 0xffff0000, v205
	v_mul_f32_e32 v14, v28, v30
	v_mul_f32_e32 v15, v29, v31
	v_lshlrev_b32_e32 v28, 16, v6
	v_and_b32_e32 v29, 0xffff0000, v6
	v_mul_f32_e32 v28, 0xbfb8aa3b, v28
	v_mul_f32_e32 v29, 0xbfb8aa3b, v29
	v_exp_f32_e32 v28, v28
	v_exp_f32_e32 v29, v29
	v_lshlrev_b32_e32 v30, 16, v206
	v_add_f32_e32 v28, 1.0, v28
	v_add_f32_e32 v29, 1.0, v29
	v_rcp_f32_e32 v28, v28
	v_rcp_f32_e32 v29, v29
	v_and_b32_e32 v31, 0xffff0000, v206
	v_mul_f32_e32 v238, v28, v30
	v_mul_f32_e32 v239, v29, v31
	v_lshlrev_b32_e32 v28, 16, v7
	v_and_b32_e32 v29, 0xffff0000, v7
	v_mul_f32_e32 v28, 0xbfb8aa3b, v28
	v_mul_f32_e32 v29, 0xbfb8aa3b, v29
	v_exp_f32_e32 v28, v28
	v_exp_f32_e32 v29, v29
	v_lshlrev_b32_e32 v30, 16, v207
	v_add_f32_e32 v28, 1.0, v28
	v_add_f32_e32 v29, 1.0, v29
	v_rcp_f32_e32 v28, v28
	v_rcp_f32_e32 v29, v29
	v_and_b32_e32 v31, 0xffff0000, v207
	v_mul_f32_e32 v240, v28, v30
	v_mul_f32_e32 v241, v29, v31
	ds_write_b128 v187, v[12:15]
	ds_write_b128 v187, v[238:241] offset:16
	v_add_u32_e32 v187, 0x4000, v187
	s_waitcnt vmcnt(2)
	v_lshlrev_b32_e32 v28, 16, v8
	v_and_b32_e32 v29, 0xffff0000, v8
	v_mul_f32_e32 v28, 0xbfb8aa3b, v28
	v_mul_f32_e32 v29, 0xbfb8aa3b, v29
	v_exp_f32_e32 v28, v28
	v_exp_f32_e32 v29, v29
	v_lshlrev_b32_e32 v30, 16, v208
	v_add_f32_e32 v28, 1.0, v28
	v_add_f32_e32 v29, 1.0, v29
	v_rcp_f32_e32 v28, v28
	v_rcp_f32_e32 v29, v29
	v_and_b32_e32 v31, 0xffff0000, v208
	v_mul_f32_e32 v12, v28, v30
	v_mul_f32_e32 v13, v29, v31
	v_lshlrev_b32_e32 v28, 16, v9
	v_and_b32_e32 v29, 0xffff0000, v9
	v_mul_f32_e32 v28, 0xbfb8aa3b, v28
	v_mul_f32_e32 v29, 0xbfb8aa3b, v29
	v_exp_f32_e32 v28, v28
	v_exp_f32_e32 v29, v29
	v_lshlrev_b32_e32 v30, 16, v209
	v_add_f32_e32 v28, 1.0, v28
	v_add_f32_e32 v29, 1.0, v29
	v_rcp_f32_e32 v28, v28
	v_rcp_f32_e32 v29, v29
	v_and_b32_e32 v31, 0xffff0000, v209
	v_mul_f32_e32 v14, v28, v30
	v_mul_f32_e32 v15, v29, v31
	v_lshlrev_b32_e32 v28, 16, v10
	v_and_b32_e32 v29, 0xffff0000, v10
	v_mul_f32_e32 v28, 0xbfb8aa3b, v28
	v_mul_f32_e32 v29, 0xbfb8aa3b, v29
	v_exp_f32_e32 v28, v28
	v_exp_f32_e32 v29, v29
	v_lshlrev_b32_e32 v30, 16, v210
	v_add_f32_e32 v28, 1.0, v28
	v_add_f32_e32 v29, 1.0, v29
	v_rcp_f32_e32 v28, v28
	v_rcp_f32_e32 v29, v29
	v_and_b32_e32 v31, 0xffff0000, v210
	v_mul_f32_e32 v238, v28, v30
	v_mul_f32_e32 v239, v29, v31
	v_lshlrev_b32_e32 v28, 16, v11
	v_and_b32_e32 v29, 0xffff0000, v11
	v_mul_f32_e32 v28, 0xbfb8aa3b, v28
	v_mul_f32_e32 v29, 0xbfb8aa3b, v29
	v_exp_f32_e32 v28, v28
	v_exp_f32_e32 v29, v29
	v_lshlrev_b32_e32 v30, 16, v211
	v_add_f32_e32 v28, 1.0, v28
	v_add_f32_e32 v29, 1.0, v29
	v_rcp_f32_e32 v28, v28
	v_rcp_f32_e32 v29, v29
	v_and_b32_e32 v31, 0xffff0000, v211
	v_mul_f32_e32 v240, v28, v30
	v_mul_f32_e32 v241, v29, v31
	ds_write_b128 v187, v[12:15]
	ds_write_b128 v187, v[238:241] offset:16
	v_add_u32_e32 v187, 0x4000, v187
	s_waitcnt vmcnt(0)
	v_lshlrev_b32_e32 v28, 16, v16
	v_and_b32_e32 v29, 0xffff0000, v16
	v_mul_f32_e32 v28, 0xbfb8aa3b, v28
	v_mul_f32_e32 v29, 0xbfb8aa3b, v29
	v_exp_f32_e32 v28, v28
	v_exp_f32_e32 v29, v29
	v_lshlrev_b32_e32 v30, 16, v212
	v_add_f32_e32 v28, 1.0, v28
	v_add_f32_e32 v29, 1.0, v29
	v_rcp_f32_e32 v28, v28
	v_rcp_f32_e32 v29, v29
	v_and_b32_e32 v31, 0xffff0000, v212
	v_mul_f32_e32 v12, v28, v30
	v_mul_f32_e32 v13, v29, v31
	v_lshlrev_b32_e32 v28, 16, v17
	v_and_b32_e32 v29, 0xffff0000, v17
	v_mul_f32_e32 v28, 0xbfb8aa3b, v28
	v_mul_f32_e32 v29, 0xbfb8aa3b, v29
	v_exp_f32_e32 v28, v28
	v_exp_f32_e32 v29, v29
	v_lshlrev_b32_e32 v30, 16, v213
	v_add_f32_e32 v28, 1.0, v28
	v_add_f32_e32 v29, 1.0, v29
	v_rcp_f32_e32 v28, v28
	v_rcp_f32_e32 v29, v29
	v_and_b32_e32 v31, 0xffff0000, v213
	v_mul_f32_e32 v14, v28, v30
	v_mul_f32_e32 v15, v29, v31
	v_lshlrev_b32_e32 v28, 16, v18
	v_and_b32_e32 v29, 0xffff0000, v18
	v_mul_f32_e32 v28, 0xbfb8aa3b, v28
	v_mul_f32_e32 v29, 0xbfb8aa3b, v29
	v_exp_f32_e32 v28, v28
	v_exp_f32_e32 v29, v29
	v_lshlrev_b32_e32 v30, 16, v214
	v_add_f32_e32 v28, 1.0, v28
	v_add_f32_e32 v29, 1.0, v29
	v_rcp_f32_e32 v28, v28
	v_rcp_f32_e32 v29, v29
	v_and_b32_e32 v31, 0xffff0000, v214
	v_mul_f32_e32 v238, v28, v30
	v_mul_f32_e32 v239, v29, v31
	v_lshlrev_b32_e32 v28, 16, v19
	v_and_b32_e32 v29, 0xffff0000, v19
	v_mul_f32_e32 v28, 0xbfb8aa3b, v28
	v_mul_f32_e32 v29, 0xbfb8aa3b, v29
	v_exp_f32_e32 v28, v28
	v_exp_f32_e32 v29, v29
	v_lshlrev_b32_e32 v30, 16, v215
	v_add_f32_e32 v28, 1.0, v28
	v_add_f32_e32 v29, 1.0, v29
	v_rcp_f32_e32 v28, v28
	v_rcp_f32_e32 v29, v29
	v_and_b32_e32 v31, 0xffff0000, v215
	v_mul_f32_e32 v240, v28, v30
	v_mul_f32_e32 v241, v29, v31
	ds_write_b128 v187, v[12:15]
	ds_write_b128 v187, v[238:241] offset:16
	s_branch .LBB0_829
